# attention tile loops: priority raised over each wave's QK and PV MFMA runs and dropped for the softmax VALU, replacing the static younger-half raise
# speedup vs baseline: 1.0144x; 1.0144x over previous
.LBB0_434:
	v_mov_b32_e32 v2, v0
	s_nop 0
	v_readfirstlane_b32 s3, v2
	s_ashr_i32 s19, s3, 6
	s_cmp_lt_i32 s19, 4
	s_cbranch_scc1 .LBB0_436
	s_nop 0

.LBB0_447:
	s_add_i32 s2, s26, s23
	s_and_b32 s3, s30, 0x18000
	s_add_i32 s3, s3, 0
	s_add_i32 s33, s3, s27
	v_add_u32_e32 v2, s33, v162
	v_add_u32_e32 v4, s33, v164
	v_add_u32_e32 v5, s33, v165
	v_add_u32_e32 v70, s33, v166
	s_ashr_i32 s33, s31, 2
	v_cvt_f32_i32_e32 v170, s33
	v_add_u32_e32 v106, s3, v160
	s_add_i32 s3, s2, 0x7e0
	v_add_u32_e32 v169, 0x4000, v106
	s_cmp_gt_i32 s3, s28
	v_add_u32_e32 v174, v2, v145
	v_add_u32_e32 v173, v4, v145
	v_add_u32_e32 v172, v5, v145
	v_add_u32_e32 v171, v70, v145
	s_barrier
	s_cbranch_scc1 .LBB0_455
	ds_read_b128 v[70:73], v174 offset:4096
	ds_read_b128 v[188:191], v173 offset:4096
	ds_read_b128 v[192:195], v172 offset:4096
	ds_read_b128 v[202:205], v171 offset:4096
	s_and_b32 s3, s3, 0xe0
	v_or_b32_e32 v2, s3, v159
	v_cvt_f32_ubyte0_e32 v2, v2
	v_and_b32_e32 v2, 0x7fff0000, v2
	v_or_b32_sdwa v2, v2, v170 dst_sel:DWORD dst_unused:UNUSED_PAD src0_sel:DWORD src1_sel:WORD_1
	v_cndmask_b32_e64 v2, 0, v2, s[36:37]
	v_mov_b32_e32 v4, v3
	s_waitcnt lgkmcnt(3)
	s_setprio 1
	v_mfma_f32_32x32x16_bf16 v[70:85], v[70:73], v[86:89], 0
	v_mov_b32_e32 v5, v3
	s_add_i32 s3, s2, 0x7ff
	s_cmp_ge_i32 s19, s3
	s_cselect_b64 s[40:41], -1, 0
	s_add_i32 s3, s29, 0xffffffa0
	s_cmp_lt_i32 s3, 0x3fffffe1
	v_add_u32_e32 v175, v169, v150
	s_waitcnt lgkmcnt(2)
	v_mfma_f32_32x32x16_bf16 v[70:85], v[188:191], v[90:93], v[70:85]
	s_cselect_b64 s[42:43], -1, 0
	s_and_b64 s[40:41], s[40:41], s[42:43]
	s_and_b64 vcc, exec, s[40:41]
	s_waitcnt lgkmcnt(1)
	v_mfma_f32_32x32x16_bf16 v[70:85], v[192:195], v[94:97], v[70:85]
	s_waitcnt lgkmcnt(0)
	v_mfma_f32_32x32x16_bf16 v[70:85], v[202:205], v[98:101], v[70:85]
	v_mfma_f32_32x32x16_bf16 v[70:85], v[2:5], v[102:105], v[70:85]
	s_setprio 0
	v_add3_u32 v2, v106, v142, s68
	v_add_u32_e32 v4, v169, v146
	v_add_u32_e32 v5, v169, v148
	ds_read_b64_tr_b16 v[134:135], v2
	ds_read_b64_tr_b16 v[136:137], v2 offset:2048
	ds_read_b64_tr_b16 v[130:131], v4
	ds_read_b64_tr_b16 v[132:133], v4 offset:2048
	ds_read_b64_tr_b16 v[126:127], v5
	ds_read_b64_tr_b16 v[128:129], v5 offset:2048
	ds_read_b64_tr_b16 v[122:123], v175
	ds_read_b64_tr_b16 v[124:125], v175 offset:2048
	ds_read_b64_tr_b16 v[118:119], v2 offset:4096
	ds_read_b64_tr_b16 v[120:121], v2 offset:6144
	ds_read_b64_tr_b16 v[114:115], v4 offset:4096
	ds_read_b64_tr_b16 v[116:117], v4 offset:6144
	ds_read_b64_tr_b16 v[110:111], v5 offset:4096
	ds_read_b64_tr_b16 v[112:113], v5 offset:6144
	ds_read_b64_tr_b16 v[106:107], v175 offset:4096
	ds_read_b64_tr_b16 v[108:109], v175 offset:6144
	s_cbranch_vccnz .LBB0_452
	v_add_u32_e32 v2, s29, v161
	v_add_u32_e32 v4, 0xffffffa0, v2
	v_cmp_gt_u32_e32 vcc, 2.0, v4
	v_add_u32_e32 v4, s23, v163
	v_add_u32_e32 v4, 0x60, v4
	s_nop 2
	v_cndmask_b32_e32 v70, v197, v70, vcc
	v_cmp_lt_u32_e32 vcc, s75, v4
	v_add_u32_e32 v4, 0xffffff9e, v2
	s_nop 0
	v_cndmask_b32_e32 v71, v197, v71, vcc
	v_cmp_gt_u32_e32 vcc, 2.0, v4
	v_add_u32_e32 v4, 0xffffff9d, v2
	s_nop 0
	v_cndmask_b32_e32 v72, v197, v72, vcc
	v_cmp_gt_u32_e32 vcc, 2.0, v4
	v_add_u32_e32 v4, 0xffffff98, v2
	s_nop 0
	v_cndmask_b32_e32 v73, v197, v73, vcc
	v_cmp_gt_u32_e32 vcc, 2.0, v4
	v_add_u32_e32 v4, 0xffffff97, v2
	s_nop 0
	v_cndmask_b32_e32 v74, v197, v74, vcc
	v_cmp_gt_u32_e32 vcc, 2.0, v4
	v_add_u32_e32 v4, 0xffffff96, v2
	s_nop 0
	v_cndmask_b32_e32 v75, v197, v75, vcc
	v_cmp_gt_u32_e32 vcc, 2.0, v4
	v_add_u32_e32 v4, 0xffffff95, v2
	s_nop 0
	v_cndmask_b32_e32 v76, v197, v76, vcc
	v_cmp_gt_u32_e32 vcc, 2.0, v4
	v_add_u32_e32 v4, 0xffffff90, v2
	s_nop 0
	v_cndmask_b32_e32 v77, v197, v77, vcc
	v_cmp_gt_u32_e32 vcc, 2.0, v4
	v_add_u32_e32 v4, 0xffffff8f, v2
	s_nop 0
	v_cndmask_b32_e32 v78, v197, v78, vcc
	v_cmp_gt_u32_e32 vcc, 2.0, v4
	v_add_u32_e32 v4, 0xffffff8e, v2
	s_nop 0
	v_cndmask_b32_e32 v79, v197, v79, vcc
	v_cmp_gt_u32_e32 vcc, 2.0, v4
	v_add_u32_e32 v4, 0xffffff8d, v2
	s_nop 0
	v_cndmask_b32_e32 v80, v197, v80, vcc
	v_cmp_gt_u32_e32 vcc, 2.0, v4
	v_add_u32_e32 v4, 0xffffff88, v2
	s_nop 0
	v_cndmask_b32_e32 v81, v197, v81, vcc
	v_cmp_gt_u32_e32 vcc, 2.0, v4
	v_add_u32_e32 v4, 0xffffff87, v2
	s_nop 0
	v_cndmask_b32_e32 v82, v197, v82, vcc
	v_cmp_gt_u32_e32 vcc, 2.0, v4
	v_add_u32_e32 v4, 0xffffff86, v2
	v_add_u32_e32 v2, 0xffffff85, v2
	v_cndmask_b32_e32 v83, v197, v83, vcc
	v_cmp_gt_u32_e32 vcc, 2.0, v4
	s_nop 1
	v_cndmask_b32_e32 v84, v197, v84, vcc
	v_cmp_gt_u32_e32 vcc, 2.0, v2
	s_nop 1
	v_cndmask_b32_e32 v85, v197, v85, vcc

.LBB0_454:
	v_mul_f32_e32 v2, 0xbfb8aa3b, v168
	v_fmamk_f32 v4, v70, 0x3fb8aa3b, v2
	v_fmamk_f32 v70, v72, 0x3fb8aa3b, v2
	v_exp_f32_e32 v176, v70
	v_fmamk_f32 v70, v73, 0x3fb8aa3b, v2
	v_exp_f32_e32 v177, v70
	v_fmamk_f32 v70, v74, 0x3fb8aa3b, v2
	v_exp_f32_e32 v74, v70
	v_fmamk_f32 v70, v75, 0x3fb8aa3b, v2
	v_exp_f32_e32 v75, v70
	v_fmamk_f32 v70, v76, 0x3fb8aa3b, v2
	v_fmamk_f32 v5, v71, 0x3fb8aa3b, v2
	v_exp_f32_e32 v76, v70
	v_fmamk_f32 v70, v77, 0x3fb8aa3b, v2
	v_exp_f32_e32 v4, v4
	v_exp_f32_e32 v5, v5
	v_exp_f32_e32 v77, v70
	v_cvt_pk_bf16_f32 v70, v4, v5
	v_cvt_pk_bf16_f32 v71, v176, v177
	v_cvt_pk_bf16_f32 v72, v74, v75
	v_cvt_pk_bf16_f32 v73, v76, v77
	v_fmamk_f32 v78, v78, 0x3fb8aa3b, v2
	s_waitcnt lgkmcnt(0)
	s_setprio 1
	v_mfma_f32_32x32x16_bf16 v[54:69], v[134:137], v[70:73], v[54:69]
	v_fmamk_f32 v79, v79, 0x3fb8aa3b, v2
	v_exp_f32_e32 v78, v78
	v_exp_f32_e32 v79, v79
	v_fmamk_f32 v80, v80, 0x3fb8aa3b, v2
	v_fmamk_f32 v81, v81, 0x3fb8aa3b, v2
	v_pk_add_f32 v[4:5], v[4:5], 0 op_sel_hi:[1,0]
	v_exp_f32_e32 v80, v80
	v_mfma_f32_32x32x16_bf16 v[38:53], v[130:133], v[70:73], v[38:53]
	v_exp_f32_e32 v81, v81
	v_fmamk_f32 v82, v82, 0x3fb8aa3b, v2
	v_fmamk_f32 v83, v83, 0x3fb8aa3b, v2
	v_fmamk_f32 v84, v84, 0x3fb8aa3b, v2
	v_fmac_f32_e32 v2, 0x3fb8aa3b, v85
	v_pk_add_f32 v[4:5], v[176:177], v[4:5]
	v_exp_f32_e32 v82, v82
	v_mfma_f32_32x32x16_bf16 v[22:37], v[126:129], v[70:73], v[22:37]
	v_exp_f32_e32 v83, v83
	v_exp_f32_e32 v84, v84
	v_exp_f32_e32 v85, v2
	v_pk_add_f32 v[4:5], v[74:75], v[4:5]
	s_nop 0
	v_pk_add_f32 v[4:5], v[76:77], v[4:5]
	v_mfma_f32_32x32x16_bf16 v[6:21], v[122:125], v[70:73], v[6:21]
	v_cvt_pk_bf16_f32 v70, v78, v79
	v_cvt_pk_bf16_f32 v71, v80, v81
	v_cvt_pk_bf16_f32 v72, v82, v83
	v_cvt_pk_bf16_f32 v73, v84, v85
	v_add_f32_e64 v4, v78, v4
	v_add_f32_e64 v5, v79, v5
	v_add_f32_e64 v4, v80, v4
	v_add_f32_e64 v5, v81, v5
	v_mfma_f32_32x32x16_bf16 v[54:69], v[118:121], v[70:73], v[54:69]
	v_add_f32_e64 v4, v82, v4
	v_add_f32_e64 v5, v83, v5
	v_add_f32_e64 v4, v84, v4
	v_add_f32_e64 v5, v85, v5
	v_add_f32_e32 v2, v4, v5
	v_add_f32_e32 v167, v167, v2
	v_mfma_f32_32x32x16_bf16 v[38:53], v[114:117], v[70:73], v[38:53]
	v_mfma_f32_32x32x16_bf16 v[22:37], v[110:113], v[70:73], v[22:37]
	v_mfma_f32_32x32x16_bf16 v[6:21], v[106:109], v[70:73], v[6:21]
	s_setprio 0

.Lring_issue_skip_2:
	s_add_i32 s3, s2, 0x7c0
	s_cmp_gt_i32 s3, s28
	s_cbranch_scc1 .LBB0_461
	ds_read_b128 v[70:73], v174
	ds_read_b128 v[188:191], v173
	ds_read_b128 v[192:195], v172
	ds_read_b128 v[202:205], v171
	s_and_b32 s3, s3, 0xc0
	v_or_b32_e32 v2, s3, v159
	v_cvt_f32_ubyte0_e32 v2, v2
	v_and_b32_e32 v2, 0x7fff0000, v2
	v_or_b32_sdwa v2, v2, v170 dst_sel:DWORD dst_unused:UNUSED_PAD src0_sel:DWORD src1_sel:WORD_1
	v_cndmask_b32_e64 v2, 0, v2, s[36:37]
	v_mov_b32_e32 v4, v3
	s_waitcnt lgkmcnt(3)
	s_setprio 1
	v_mfma_f32_32x32x16_bf16 v[70:85], v[70:73], v[86:89], 0
	v_mov_b32_e32 v5, v3
	s_addk_i32 s2, 0x7df
	s_cmp_ge_i32 s19, s2
	s_cselect_b64 s[2:3], -1, 0
	s_sub_i32 s33, s29, 64
	s_cmp_lt_i32 s33, 0x3fffffe1
	s_cselect_b64 s[40:41], -1, 0
	s_waitcnt lgkmcnt(2)
	v_mfma_f32_32x32x16_bf16 v[70:85], v[188:191], v[90:93], v[70:85]
	s_and_b64 s[2:3], s[2:3], s[40:41]
	s_and_b64 vcc, exec, s[2:3]
	s_waitcnt lgkmcnt(1)
	v_mfma_f32_32x32x16_bf16 v[70:85], v[192:195], v[94:97], v[70:85]
	s_waitcnt lgkmcnt(0)
	v_mfma_f32_32x32x16_bf16 v[70:85], v[202:205], v[98:101], v[70:85]
	v_mfma_f32_32x32x16_bf16 v[70:85], v[2:5], v[102:105], v[70:85]
	s_setprio 0
	v_add_u32_e32 v2, v169, v142
	v_add_u32_e32 v4, v169, v152
	v_add_u32_e32 v5, v169, v154
	v_add_u32_e32 v169, v169, v156
	ds_read_b64_tr_b16 v[134:135], v2
	ds_read_b64_tr_b16 v[136:137], v2 offset:2048
	ds_read_b64_tr_b16 v[130:131], v4
	ds_read_b64_tr_b16 v[132:133], v4 offset:2048
	ds_read_b64_tr_b16 v[126:127], v5
	ds_read_b64_tr_b16 v[128:129], v5 offset:2048
	ds_read_b64_tr_b16 v[122:123], v169
	ds_read_b64_tr_b16 v[124:125], v169 offset:2048
	ds_read_b64_tr_b16 v[118:119], v2 offset:4096
	ds_read_b64_tr_b16 v[120:121], v2 offset:6144
	ds_read_b64_tr_b16 v[114:115], v4 offset:4096
	ds_read_b64_tr_b16 v[116:117], v4 offset:6144
	ds_read_b64_tr_b16 v[110:111], v5 offset:4096
	ds_read_b64_tr_b16 v[112:113], v5 offset:6144
	ds_read_b64_tr_b16 v[106:107], v169 offset:4096
	ds_read_b64_tr_b16 v[108:109], v169 offset:6144
	s_cbranch_vccnz .LBB0_458
	v_add_u32_e32 v2, s29, v161
	v_subrev_u32_e32 v4, 64, v2
	v_cmp_gt_u32_e32 vcc, 2.0, v4
	v_add3_u32 v4, v163, s23, 64
	s_nop 2
	v_cndmask_b32_e32 v70, v197, v70, vcc
	v_cmp_lt_u32_e32 vcc, s75, v4
	v_add_u32_e32 v4, 0xffffffbe, v2
	s_nop 0
	v_cndmask_b32_e32 v71, v197, v71, vcc
	v_cmp_gt_u32_e32 vcc, 2.0, v4
	v_add_u32_e32 v4, 0xffffffbd, v2
	s_nop 0
	v_cndmask_b32_e32 v72, v197, v72, vcc
	v_cmp_gt_u32_e32 vcc, 2.0, v4
	v_add_u32_e32 v4, 0xffffffb8, v2
	s_nop 0
	v_cndmask_b32_e32 v73, v197, v73, vcc
	v_cmp_gt_u32_e32 vcc, 2.0, v4
	v_add_u32_e32 v4, 0xffffffb7, v2
	s_nop 0
	v_cndmask_b32_e32 v74, v197, v74, vcc
	v_cmp_gt_u32_e32 vcc, 2.0, v4
	v_add_u32_e32 v4, 0xffffffb6, v2
	s_nop 0
	v_cndmask_b32_e32 v75, v197, v75, vcc
	v_cmp_gt_u32_e32 vcc, 2.0, v4
	v_add_u32_e32 v4, 0xffffffb5, v2
	s_nop 0
	v_cndmask_b32_e32 v76, v197, v76, vcc
	v_cmp_gt_u32_e32 vcc, 2.0, v4
	v_add_u32_e32 v4, 0xffffffb0, v2
	s_nop 0
	v_cndmask_b32_e32 v77, v197, v77, vcc
	v_cmp_gt_u32_e32 vcc, 2.0, v4
	v_add_u32_e32 v4, 0xffffffaf, v2
	s_nop 0
	v_cndmask_b32_e32 v78, v197, v78, vcc
	v_cmp_gt_u32_e32 vcc, 2.0, v4
	v_add_u32_e32 v4, 0xffffffae, v2
	s_nop 0
	v_cndmask_b32_e32 v79, v197, v79, vcc
	v_cmp_gt_u32_e32 vcc, 2.0, v4
	v_add_u32_e32 v4, 0xffffffad, v2
	s_nop 0
	v_cndmask_b32_e32 v80, v197, v80, vcc
	v_cmp_gt_u32_e32 vcc, 2.0, v4
	v_add_u32_e32 v4, 0xffffffa8, v2
	s_nop 0
	v_cndmask_b32_e32 v81, v197, v81, vcc
	v_cmp_gt_u32_e32 vcc, 2.0, v4
	v_add_u32_e32 v4, 0xffffffa7, v2
	s_nop 0
	v_cndmask_b32_e32 v82, v197, v82, vcc
	v_cmp_gt_u32_e32 vcc, 2.0, v4
	v_add_u32_e32 v4, 0xffffffa6, v2
	v_add_u32_e32 v2, 0xffffffa5, v2
	v_cndmask_b32_e32 v83, v197, v83, vcc
	v_cmp_gt_u32_e32 vcc, 2.0, v4
	s_nop 1
	v_cndmask_b32_e32 v84, v197, v84, vcc
	v_cmp_gt_u32_e32 vcc, 2.0, v2
	s_nop 1
	v_cndmask_b32_e32 v85, v197, v85, vcc

.LBB0_460:
	v_mul_f32_e32 v2, 0xbfb8aa3b, v168
	v_fmamk_f32 v4, v70, 0x3fb8aa3b, v2
	v_fmamk_f32 v70, v72, 0x3fb8aa3b, v2
	v_exp_f32_e32 v170, v70
	v_fmamk_f32 v70, v73, 0x3fb8aa3b, v2
	v_exp_f32_e32 v171, v70
	v_fmamk_f32 v70, v74, 0x3fb8aa3b, v2
	v_exp_f32_e32 v74, v70
	v_fmamk_f32 v70, v75, 0x3fb8aa3b, v2
	v_exp_f32_e32 v75, v70
	v_fmamk_f32 v70, v76, 0x3fb8aa3b, v2
	v_fmamk_f32 v5, v71, 0x3fb8aa3b, v2
	v_exp_f32_e32 v76, v70
	v_fmamk_f32 v70, v77, 0x3fb8aa3b, v2
	v_exp_f32_e32 v4, v4
	v_exp_f32_e32 v5, v5
	v_exp_f32_e32 v77, v70
	v_cvt_pk_bf16_f32 v70, v4, v5
	v_cvt_pk_bf16_f32 v71, v170, v171
	v_cvt_pk_bf16_f32 v72, v74, v75
	v_cvt_pk_bf16_f32 v73, v76, v77
	v_fmamk_f32 v78, v78, 0x3fb8aa3b, v2
	s_waitcnt lgkmcnt(0)
	s_setprio 1
	v_mfma_f32_32x32x16_bf16 v[54:69], v[134:137], v[70:73], v[54:69]
	v_fmamk_f32 v79, v79, 0x3fb8aa3b, v2
	v_exp_f32_e32 v78, v78
	v_exp_f32_e32 v79, v79
	v_fmamk_f32 v80, v80, 0x3fb8aa3b, v2
	v_fmamk_f32 v81, v81, 0x3fb8aa3b, v2
	v_pk_add_f32 v[4:5], v[4:5], 0 op_sel_hi:[1,0]
	v_exp_f32_e32 v80, v80
	v_mfma_f32_32x32x16_bf16 v[38:53], v[130:133], v[70:73], v[38:53]
	v_exp_f32_e32 v81, v81
	v_fmamk_f32 v82, v82, 0x3fb8aa3b, v2
	v_fmamk_f32 v83, v83, 0x3fb8aa3b, v2
	v_fmamk_f32 v84, v84, 0x3fb8aa3b, v2
	v_fmac_f32_e32 v2, 0x3fb8aa3b, v85
	v_pk_add_f32 v[4:5], v[170:171], v[4:5]
	v_exp_f32_e32 v82, v82
	v_mfma_f32_32x32x16_bf16 v[22:37], v[126:129], v[70:73], v[22:37]
	v_exp_f32_e32 v83, v83
	v_exp_f32_e32 v84, v84
	v_exp_f32_e32 v85, v2
	v_pk_add_f32 v[4:5], v[74:75], v[4:5]
	s_nop 0
	v_pk_add_f32 v[4:5], v[76:77], v[4:5]
	v_mfma_f32_32x32x16_bf16 v[6:21], v[122:125], v[70:73], v[6:21]
	v_cvt_pk_bf16_f32 v70, v78, v79
	v_cvt_pk_bf16_f32 v71, v80, v81
	v_cvt_pk_bf16_f32 v72, v82, v83
	v_cvt_pk_bf16_f32 v73, v84, v85
	v_add_f32_e64 v4, v78, v4
	v_add_f32_e64 v5, v79, v5
	v_add_f32_e64 v4, v80, v4
	v_add_f32_e64 v5, v81, v5
	v_mfma_f32_32x32x16_bf16 v[54:69], v[118:121], v[70:73], v[54:69]
	v_add_f32_e64 v4, v82, v4
	v_add_f32_e64 v5, v83, v5
	v_add_f32_e64 v4, v84, v4
	v_add_f32_e64 v5, v85, v5
	v_add_f32_e32 v2, v4, v5
	v_add_f32_e32 v167, v167, v2
	v_mfma_f32_32x32x16_bf16 v[38:53], v[114:117], v[70:73], v[38:53]
	v_mfma_f32_32x32x16_bf16 v[22:37], v[110:113], v[70:73], v[22:37]
	v_mfma_f32_32x32x16_bf16 v[6:21], v[106:109], v[70:73], v[6:21]
	s_setprio 0

.LBB0_502:
	s_or_b64 exec, exec, s[2:3]
	v_mov_b32_e32 v4, v0
	s_nop 0
	v_readfirstlane_b32 s19, v4
	s_ashr_i32 s18, s19, 6
	s_cmp_lt_i32 s18, 4
	s_cbranch_scc1 .LBB0_504
	s_nop 0

.LBB0_509:
	v_mul_f32_e32 v2, 0xbfb8aa3b, v110
	v_fmamk_f32 v16, v50, 0x3fb8aa3b, v2
	v_fmamk_f32 v50, v52, 0x3fb8aa3b, v2
	v_exp_f32_e32 v52, v50
	v_fmamk_f32 v50, v53, 0x3fb8aa3b, v2
	v_exp_f32_e32 v53, v50
	v_fmamk_f32 v50, v54, 0x3fb8aa3b, v2
	v_exp_f32_e32 v54, v50
	v_fmamk_f32 v50, v55, 0x3fb8aa3b, v2
	v_exp_f32_e32 v55, v50
	v_fmamk_f32 v50, v56, 0x3fb8aa3b, v2
	v_exp_f32_e32 v56, v50
	v_fmamk_f32 v50, v57, 0x3fb8aa3b, v2
	v_exp_f32_e32 v57, v50
	v_fmamk_f32 v50, v58, 0x3fb8aa3b, v2
	v_exp_f32_e32 v58, v50
	v_fmamk_f32 v50, v59, 0x3fb8aa3b, v2
	v_fmamk_f32 v17, v51, 0x3fb8aa3b, v2
	v_exp_f32_e32 v59, v50
	v_fmamk_f32 v50, v60, 0x3fb8aa3b, v2
	v_exp_f32_e32 v16, v16
	v_exp_f32_e32 v17, v17
	v_exp_f32_e32 v60, v50
	v_fmamk_f32 v50, v61, 0x3fb8aa3b, v2
	v_exp_f32_e32 v61, v50
	v_fmamk_f32 v50, v62, 0x3fb8aa3b, v2
	v_exp_f32_e32 v62, v50
	v_fmamk_f32 v50, v63, 0x3fb8aa3b, v2
	v_exp_f32_e32 v63, v50
	v_fmamk_f32 v50, v64, 0x3fb8aa3b, v2
	v_exp_f32_e32 v64, v50
	v_fmac_f32_e32 v2, 0x3fb8aa3b, v65
	v_pk_add_f32 v[50:51], v[16:17], v[52:53]
	v_exp_f32_e32 v65, v2
	v_pk_add_f32 v[244:245], v[54:55], v[56:57]
	v_pk_add_f32 v[50:51], v[58:59], v[50:51]
	v_pk_add_f32 v[244:245], v[60:61], v[244:245]
	v_pk_add_f32 v[50:51], v[62:63], v[50:51]
	v_pk_add_f32 v[244:245], v[64:65], v[244:245]
	s_nop 0
	v_pk_add_f32 v[50:51], v[50:51], v[244:245]
	s_nop 0
	v_add_f32_e32 v2, v50, v51
	v_cvt_pk_bf16_f32 v50, v16, v17
	v_cvt_pk_bf16_f32 v51, v52, v53
	v_cvt_pk_bf16_f32 v52, v54, v55
	v_cvt_pk_bf16_f32 v53, v56, v57
	v_add_f32_e32 v107, v107, v2
	s_waitcnt lgkmcnt(0)
	s_setprio 1
	v_mfma_f32_32x32x16_bf16 v[34:49], v[86:89], v[50:53], v[34:49]
	v_mfma_f32_32x32x16_bf16 v[18:33], v[12:15], v[50:53], v[18:33]
	v_cvt_pk_bf16_f32 v12, v58, v59
	v_cvt_pk_bf16_f32 v13, v60, v61
	v_cvt_pk_bf16_f32 v14, v62, v63
	v_cvt_pk_bf16_f32 v15, v64, v65
	s_nop 0
	v_mfma_f32_32x32x16_bf16 v[34:49], v[8:11], v[12:15], v[34:49]
	v_mfma_f32_32x32x16_bf16 v[18:33], v[4:7], v[12:15], v[18:33]
	s_setprio 0

.Lw_win_4_done:
.LBB0_519:
	s_cmp_eq_u32 s32, 0
	s_cselect_b32 s84, 0, 1
	s_sub_u32 s32, s32, s84
	s_add_i32 s2, s29, s22
	s_add_i32 s3, s27, s21
	s_add_i32 s3, s3, -1
	s_and_b32 s31, s30, 0xc000
	s_add_i32 s33, s31, 0
	s_ashr_i32 s3, s3, 2
	s_add_i32 s31, s2, 0x7e0
	s_cmp_gt_i32 s31, s23
	v_cvt_f32_i32_e32 v111, s3
	s_cselect_b64 s[34:35], -1, 0
	s_add_i32 s3, s2, 0x7ff
	s_cmp_lt_i32 s3, s24
	s_cselect_b64 s[38:39], -1, 0
	v_add_u32_e32 v2, s33, v101
	v_add_u32_e32 v4, s33, v102
	v_add_u32_e32 v5, s33, v103
	v_add_u32_e32 v6, s33, v104
	s_or_b64 s[34:35], s[34:35], s[38:39]
	s_and_b64 vcc, exec, s[34:35]
	v_add_u32_e32 v115, v2, v100
	v_add_u32_e32 v114, v4, v100
	v_add_u32_e32 v113, v5, v100
	v_add_u32_e32 v112, v6, v100
	v_add_u32_e32 v16, s33, v105
	v_add_u32_e32 v17, s33, v106
	s_barrier
	s_cbranch_vccnz .LBB0_527
	ds_read_b128 v[4:7], v115 offset:4096
	ds_read_b128 v[188:191], v114 offset:4096
	ds_read_b128 v[192:195], v113 offset:4096
	ds_read_b128 v[202:205], v112 offset:4096
	s_and_b32 s31, s31, 0xe0
	v_or_b32_e32 v2, s31, v99
	v_cvt_f32_ubyte0_e32 v2, v2
	v_and_b32_e32 v2, 0x7fff0000, v2
	v_or_b32_sdwa v2, v2, v111 dst_sel:DWORD dst_unused:UNUSED_PAD src0_sel:DWORD src1_sel:WORD_1
	v_cndmask_b32_e64 v246, 0, v2, s[36:37]
	s_cmp_ge_i32 s20, s3
	s_cselect_b64 s[34:35], -1, 0
	s_waitcnt lgkmcnt(3)
	s_setprio 1
	v_mfma_f32_32x32x16_bf16 v[50:65], v[4:7], v[74:77], 0
	s_sub_i32 s3, s19, 32
	s_cmpk_lt_i32 s3, 0x1e1
	v_add3_u32 v116, v17, v94, s69
	s_cselect_b64 s[38:39], -1, 0
	s_and_b64 s[34:35], s[34:35], s[38:39]
	s_and_b64 vcc, exec, s[34:35]
	s_waitcnt lgkmcnt(2)
	v_mfma_f32_32x32x16_bf16 v[50:65], v[188:191], v[66:69], v[50:65]
	s_waitcnt lgkmcnt(1)
	v_mfma_f32_32x32x16_bf16 v[50:65], v[192:195], v[70:73], v[50:65]
	s_waitcnt lgkmcnt(0)
	v_mfma_f32_32x32x16_bf16 v[50:65], v[202:205], v[78:81], v[50:65]
	v_mfma_f32_32x32x16_bf16 v[50:65], v[246:249], v[82:85], v[50:65]
	s_setprio 0
	v_add3_u32 v2, v16, v94, s69
	ds_read_b64_tr_b16 v[86:87], v2
	ds_read_b64_tr_b16 v[88:89], v2 offset:1024
	ds_read_b64_tr_b16 v[12:13], v116
	ds_read_b64_tr_b16 v[14:15], v116 offset:1024
	ds_read_b64_tr_b16 v[8:9], v2 offset:2048
	ds_read_b64_tr_b16 v[10:11], v2 offset:3072
	ds_read_b64_tr_b16 v[4:5], v116 offset:2048
	ds_read_b64_tr_b16 v[6:7], v116 offset:3072
	s_cbranch_vccnz .LBB0_524
	v_add_u32_e32 v2, s19, v108
	v_subrev_u32_e32 v116, 32, v2
	v_cmp_gt_u32_e32 vcc, s79, v116
	v_add3_u32 v116, v109, s22, 32
	s_nop 5
	v_cndmask_b32_e32 v50, v197, v50, vcc
	v_cmp_lt_u32_e32 vcc, s80, v116
	v_subrev_u32_e32 v116, 34, v2
	s_nop 0
	v_cndmask_b32_e32 v51, v197, v51, vcc
	v_cmp_gt_u32_e32 vcc, s79, v116
	v_subrev_u32_e32 v116, 35, v2
	s_nop 0
	v_cndmask_b32_e32 v52, v197, v52, vcc
	v_cmp_gt_u32_e32 vcc, s79, v116
	v_subrev_u32_e32 v116, 40, v2
	s_nop 0
	v_cndmask_b32_e32 v53, v197, v53, vcc
	v_cmp_gt_u32_e32 vcc, s79, v116
	v_subrev_u32_e32 v116, 41, v2
	s_nop 0
	v_cndmask_b32_e32 v54, v197, v54, vcc
	v_cmp_gt_u32_e32 vcc, s79, v116
	v_subrev_u32_e32 v116, 42, v2
	s_nop 0
	v_cndmask_b32_e32 v55, v197, v55, vcc
	v_cmp_gt_u32_e32 vcc, s79, v116
	v_subrev_u32_e32 v116, 43, v2
	s_nop 0
	v_cndmask_b32_e32 v56, v197, v56, vcc
	v_cmp_gt_u32_e32 vcc, s79, v116
	v_subrev_u32_e32 v116, 48, v2
	s_nop 0
	v_cndmask_b32_e32 v57, v197, v57, vcc
	v_cmp_gt_u32_e32 vcc, s79, v116
	v_subrev_u32_e32 v116, 49, v2
	s_nop 0
	v_cndmask_b32_e32 v58, v197, v58, vcc
	v_cmp_gt_u32_e32 vcc, s79, v116
	v_subrev_u32_e32 v116, 50, v2
	s_nop 0
	v_cndmask_b32_e32 v59, v197, v59, vcc
	v_cmp_gt_u32_e32 vcc, s79, v116
	v_subrev_u32_e32 v116, 51, v2
	s_nop 0
	v_cndmask_b32_e32 v60, v197, v60, vcc
	v_cmp_gt_u32_e32 vcc, s79, v116
	v_subrev_u32_e32 v116, 56, v2
	s_nop 0
	v_cndmask_b32_e32 v61, v197, v61, vcc
	v_cmp_gt_u32_e32 vcc, s79, v116
	v_subrev_u32_e32 v116, 57, v2
	s_nop 0
	v_cndmask_b32_e32 v62, v197, v62, vcc
	v_cmp_gt_u32_e32 vcc, s79, v116
	v_subrev_u32_e32 v116, 58, v2
	v_subrev_u32_e32 v2, 59, v2
	v_cndmask_b32_e32 v63, v197, v63, vcc
	v_cmp_gt_u32_e32 vcc, s79, v116
	s_nop 1
	v_cndmask_b32_e32 v64, v197, v64, vcc
	v_cmp_gt_u32_e32 vcc, s79, v2
	s_nop 1
	v_cndmask_b32_e32 v65, v197, v65, vcc

.LBB0_526:
	v_mul_f32_e32 v2, 0xbfb8aa3b, v110
	v_fmamk_f32 v50, v50, 0x3fb8aa3b, v2
	v_fmamk_f32 v51, v51, 0x3fb8aa3b, v2
	v_exp_f32_e32 v50, v50
	v_exp_f32_e32 v51, v51
	v_fmamk_f32 v52, v52, 0x3fb8aa3b, v2
	v_fmamk_f32 v53, v53, 0x3fb8aa3b, v2
	v_exp_f32_e32 v52, v52
	v_exp_f32_e32 v53, v53
	v_fmamk_f32 v54, v54, 0x3fb8aa3b, v2
	v_fmamk_f32 v55, v55, 0x3fb8aa3b, v2
	v_fmamk_f32 v56, v56, 0x3fb8aa3b, v2
	v_fmamk_f32 v57, v57, 0x3fb8aa3b, v2
	v_pk_add_f32 v[116:117], v[50:51], 0 op_sel_hi:[1,0]
	v_exp_f32_e32 v54, v54
	v_exp_f32_e32 v55, v55
	v_exp_f32_e32 v56, v56
	v_exp_f32_e32 v57, v57
	v_pk_add_f32 v[116:117], v[52:53], v[116:117]
	v_cvt_pk_bf16_f32 v50, v50, v51
	v_cvt_pk_bf16_f32 v51, v52, v53
	v_cvt_pk_bf16_f32 v52, v54, v55
	v_cvt_pk_bf16_f32 v53, v56, v57
	v_fmamk_f32 v58, v58, 0x3fb8aa3b, v2
	s_waitcnt lgkmcnt(0)
	s_setprio 1
	v_mfma_f32_32x32x16_bf16 v[34:49], v[86:89], v[50:53], v[34:49]
	v_fmamk_f32 v59, v59, 0x3fb8aa3b, v2
	v_exp_f32_e32 v58, v58
	v_exp_f32_e32 v59, v59
	v_fmamk_f32 v60, v60, 0x3fb8aa3b, v2
	v_fmamk_f32 v61, v61, 0x3fb8aa3b, v2
	v_exp_f32_e32 v60, v60
	v_exp_f32_e32 v61, v61
	v_mfma_f32_32x32x16_bf16 v[18:33], v[12:15], v[50:53], v[18:33]
	v_fmamk_f32 v62, v62, 0x3fb8aa3b, v2
	v_fmamk_f32 v63, v63, 0x3fb8aa3b, v2
	v_fmamk_f32 v64, v64, 0x3fb8aa3b, v2
	v_fmac_f32_e32 v2, 0x3fb8aa3b, v65
	v_exp_f32_e32 v62, v62
	v_exp_f32_e32 v63, v63
	v_exp_f32_e32 v64, v64
	v_exp_f32_e32 v65, v2
	v_pk_add_f32 v[116:117], v[54:55], v[116:117]
	v_cvt_pk_bf16_f32 v12, v58, v59
	v_cvt_pk_bf16_f32 v13, v60, v61
	v_cvt_pk_bf16_f32 v14, v62, v63
	v_cvt_pk_bf16_f32 v15, v64, v65
	s_nop 0
	v_mfma_f32_32x32x16_bf16 v[34:49], v[8:11], v[12:15], v[34:49]
	v_add_f32_e64 v116, v56, v116
	v_add_f32_e64 v117, v57, v117
	v_add_f32_e64 v116, v58, v116
	v_add_f32_e64 v117, v59, v117
	v_add_f32_e64 v116, v60, v116
	v_add_f32_e64 v117, v61, v117
	v_pk_add_f32 v[116:117], v[62:63], v[116:117]
	v_mfma_f32_32x32x16_bf16 v[18:33], v[4:7], v[12:15], v[18:33]
	s_setprio 0
	v_add_f32_e64 v116, v64, v116
	v_add_f32_e64 v117, v65, v117
	v_add_f32_e32 v2, v116, v117
	v_add_f32_e32 v107, v107, v2

.Lring_issue_skip_0:
	s_add_i32 s3, s2, 0x7c0
	s_cmp_gt_i32 s3, s23
	s_cselect_b64 s[34:35], -1, 0
	s_addk_i32 s2, 0x7df
	s_cmp_lt_i32 s2, s24
	s_cselect_b64 s[38:39], -1, 0
	s_or_b64 s[34:35], s[34:35], s[38:39]
	s_and_b64 vcc, exec, s[34:35]
	s_cbranch_vccnz .LBB0_510
	ds_read_b128 v[4:7], v115
	ds_read_b128 v[188:191], v114
	ds_read_b128 v[192:195], v113
	ds_read_b128 v[202:205], v112
	s_and_b32 s3, s3, 0xc0
	v_or_b32_e32 v2, s3, v99
	v_cvt_f32_ubyte0_e32 v2, v2
	v_and_b32_e32 v2, 0x7fff0000, v2
	v_or_b32_sdwa v2, v2, v111 dst_sel:DWORD dst_unused:UNUSED_PAD src0_sel:DWORD src1_sel:WORD_1
	v_cndmask_b32_e64 v246, 0, v2, s[36:37]
	s_cmp_ge_i32 s20, s2
	s_cselect_b64 s[2:3], -1, 0
	s_waitcnt lgkmcnt(3)
	s_setprio 1
	v_mfma_f32_32x32x16_bf16 v[50:65], v[4:7], v[74:77], 0
	s_cmpk_lt_i32 s19, 0x1e1
	s_cselect_b64 s[34:35], -1, 0
	s_and_b64 s[2:3], s[2:3], s[34:35]
	s_and_b64 vcc, exec, s[2:3]
	s_waitcnt lgkmcnt(2)
	v_mfma_f32_32x32x16_bf16 v[50:65], v[188:191], v[66:69], v[50:65]
	s_waitcnt lgkmcnt(1)
	v_mfma_f32_32x32x16_bf16 v[50:65], v[192:195], v[70:73], v[50:65]
	s_waitcnt lgkmcnt(0)
	v_mfma_f32_32x32x16_bf16 v[50:65], v[202:205], v[78:81], v[50:65]
	v_mfma_f32_32x32x16_bf16 v[50:65], v[246:249], v[82:85], v[50:65]
	s_setprio 0
	v_add3_u32 v2, v16, v94, s67
	v_add3_u32 v16, v17, v94, s67
	ds_read_b64_tr_b16 v[86:87], v2
	ds_read_b64_tr_b16 v[88:89], v2 offset:1024
	ds_read_b64_tr_b16 v[12:13], v16
	ds_read_b64_tr_b16 v[14:15], v16 offset:1024
	ds_read_b64_tr_b16 v[8:9], v2 offset:2048
	ds_read_b64_tr_b16 v[10:11], v2 offset:3072
	ds_read_b64_tr_b16 v[4:5], v16 offset:2048
	ds_read_b64_tr_b16 v[6:7], v16 offset:3072
	s_cbranch_vccnz .LBB0_530
	v_add_u32_e32 v2, s19, v108
	v_cmp_gt_u32_e32 vcc, s79, v2
	v_add_u32_e32 v16, s22, v109
	s_nop 5
	v_cndmask_b32_e32 v50, v197, v50, vcc
	v_cmp_lt_u32_e32 vcc, s80, v16
	v_add_u32_e32 v16, -2, v2
	s_nop 0
	v_cndmask_b32_e32 v51, v197, v51, vcc
	v_cmp_gt_u32_e32 vcc, s79, v16
	v_add_u32_e32 v16, -3, v2
	s_nop 0
	v_cndmask_b32_e32 v52, v197, v52, vcc
	v_cmp_gt_u32_e32 vcc, s79, v16
	v_add_u32_e32 v16, -8, v2
	s_nop 0
	v_cndmask_b32_e32 v53, v197, v53, vcc
	v_cmp_gt_u32_e32 vcc, s79, v16
	v_add_u32_e32 v16, -9, v2
	s_nop 0
	v_cndmask_b32_e32 v54, v197, v54, vcc
	v_cmp_gt_u32_e32 vcc, s79, v16
	v_add_u32_e32 v16, -10, v2
	s_nop 0
	v_cndmask_b32_e32 v55, v197, v55, vcc
	v_cmp_gt_u32_e32 vcc, s79, v16
	v_add_u32_e32 v16, -11, v2
	s_nop 0
	v_cndmask_b32_e32 v56, v197, v56, vcc
	v_cmp_gt_u32_e32 vcc, s79, v16
	v_add_u32_e32 v16, -16, v2
	s_nop 0
	v_cndmask_b32_e32 v57, v197, v57, vcc
	v_cmp_gt_u32_e32 vcc, s79, v16
	v_subrev_u32_e32 v16, 17, v2
	s_nop 0
	v_cndmask_b32_e32 v58, v197, v58, vcc
	v_cmp_gt_u32_e32 vcc, s79, v16
	v_subrev_u32_e32 v16, 18, v2
	s_nop 0
	v_cndmask_b32_e32 v59, v197, v59, vcc
	v_cmp_gt_u32_e32 vcc, s79, v16
	v_subrev_u32_e32 v16, 19, v2
	s_nop 0
	v_cndmask_b32_e32 v60, v197, v60, vcc
	v_cmp_gt_u32_e32 vcc, s79, v16
	v_subrev_u32_e32 v16, 24, v2
	s_nop 0
	v_cndmask_b32_e32 v61, v197, v61, vcc
	v_cmp_gt_u32_e32 vcc, s79, v16
	v_subrev_u32_e32 v16, 25, v2
	s_nop 0
	v_cndmask_b32_e32 v62, v197, v62, vcc
	v_cmp_gt_u32_e32 vcc, s79, v16
	v_subrev_u32_e32 v16, 26, v2
	v_subrev_u32_e32 v2, 27, v2
	v_cndmask_b32_e32 v63, v197, v63, vcc
	v_cmp_gt_u32_e32 vcc, s79, v16
	s_nop 1
	v_cndmask_b32_e32 v64, v197, v64, vcc
	v_cmp_gt_u32_e32 vcc, s79, v2
	s_nop 1
	v_cndmask_b32_e32 v65, v197, v65, vcc

.LBB0_642:
	s_or_b64 exec, exec, s[0:1]
	v_mov_b32_e32 v2, s73
	s_waitcnt lgkmcnt(0)
	s_barrier
	ds_read_b32 v2, v2
	s_mov_b64 s[0:1], -1
	s_waitcnt lgkmcnt(0)
	v_readfirstlane_b32 s12, v2
	s_cmpk_gt_i32 s12, 0x3ff
	s_cbranch_scc1 .LBB0_637
	v_mov_b32_e32 v65, v0
	s_nop 0
	v_readfirstlane_b32 s0, v65
	s_ashr_i32 s1, s0, 6
	s_cmp_lt_i32 s1, 4
	s_cbranch_scc1 .LBB0_645
	s_nop 0

.LBB0_668:
	v_mul_f32_e32 v2, 0xbfb8aa3b, v158
	v_fmamk_f32 v16, v82, 0x3fb8aa3b, v2
	v_fmamk_f32 v82, v84, 0x3fb8aa3b, v2
	v_exp_f32_e32 v84, v82
	v_fmamk_f32 v82, v85, 0x3fb8aa3b, v2
	v_exp_f32_e32 v85, v82
	v_fmamk_f32 v82, v86, 0x3fb8aa3b, v2
	v_exp_f32_e32 v86, v82
	v_fmamk_f32 v82, v87, 0x3fb8aa3b, v2
	v_exp_f32_e32 v87, v82
	v_fmamk_f32 v82, v88, 0x3fb8aa3b, v2
	v_exp_f32_e32 v88, v82
	v_fmamk_f32 v82, v89, 0x3fb8aa3b, v2
	v_exp_f32_e32 v89, v82
	v_fmamk_f32 v82, v90, 0x3fb8aa3b, v2
	v_exp_f32_e32 v90, v82
	v_fmamk_f32 v82, v91, 0x3fb8aa3b, v2
	v_fmamk_f32 v17, v83, 0x3fb8aa3b, v2
	v_exp_f32_e32 v91, v82
	v_fmamk_f32 v82, v92, 0x3fb8aa3b, v2
	v_exp_f32_e32 v16, v16
	v_exp_f32_e32 v17, v17
	v_exp_f32_e32 v92, v82
	v_fmamk_f32 v82, v93, 0x3fb8aa3b, v2
	v_exp_f32_e32 v93, v82
	v_fmamk_f32 v82, v94, 0x3fb8aa3b, v2
	v_exp_f32_e32 v94, v82
	v_fmamk_f32 v82, v95, 0x3fb8aa3b, v2
	v_exp_f32_e32 v95, v82
	v_fmamk_f32 v82, v96, 0x3fb8aa3b, v2
	v_exp_f32_e32 v96, v82
	v_fmac_f32_e32 v2, 0x3fb8aa3b, v97
	v_pk_add_f32 v[82:83], v[16:17], v[84:85]
	v_exp_f32_e32 v97, v2
	v_pk_add_f32 v[218:219], v[86:87], v[88:89]
	v_pk_add_f32 v[82:83], v[90:91], v[82:83]
	v_pk_add_f32 v[218:219], v[92:93], v[218:219]
	v_pk_add_f32 v[82:83], v[94:95], v[82:83]
	v_pk_add_f32 v[218:219], v[96:97], v[218:219]
	s_nop 0
	v_pk_add_f32 v[82:83], v[82:83], v[218:219]
	s_nop 0
	v_add_f32_e32 v2, v82, v83
	v_cvt_pk_bf16_f32 v82, v16, v17
	v_cvt_pk_bf16_f32 v83, v84, v85
	v_cvt_pk_bf16_f32 v84, v86, v87
	v_cvt_pk_bf16_f32 v85, v88, v89
	v_add_f32_e32 v144, v144, v2
	s_waitcnt lgkmcnt(0)
	s_setprio 1
	v_mfma_f32_32x32x16_bf16 v[66:81], v[118:121], v[82:85], v[66:81]
	v_mfma_f32_32x32x16_bf16 v[50:65], v[12:15], v[82:85], v[50:65]
	v_cvt_pk_bf16_f32 v12, v90, v91
	v_cvt_pk_bf16_f32 v13, v92, v93
	v_cvt_pk_bf16_f32 v14, v94, v95
	v_cvt_pk_bf16_f32 v15, v96, v97
	s_nop 0
	v_mfma_f32_32x32x16_bf16 v[66:81], v[8:11], v[12:15], v[66:81]
	v_mfma_f32_32x32x16_bf16 v[50:65], v[4:7], v[12:15], v[50:65]
	s_setprio 0

.LBB0_681:
	s_flbit_i32_b32 s0, s2
	s_xor_b32 s0, s0, 31
	s_lshl_b32 s8, 1, s0
	s_waitcnt lgkmcnt(0)
	v_and_b32_e32 v2, s8, v136
	v_cmp_ne_u32_e64 s[38:39], 0, v2
	s_mov_b64 vcc, s[38:39]
	s_cbranch_vccz .LBB0_669
	s_and_b32 s1, s5, 0xc000
	s_lshl_b32 s9, s0, 6
	s_lshr_b32 s0, s0, 2
	s_xor_b32 s1, s1, 0x8000
	v_cvt_f32_u32_e32 v159, s0
	s_add_i32 s1, s1, 0
	v_add_u32_e32 v2, s1, v137
	v_add_u32_e32 v4, s1, v138
	v_add_u32_e32 v5, s1, v139
	v_add_u32_e32 v6, s1, v140
	s_or_b32 s10, s9, 32
	s_cmp_gt_i32 s10, s6
	v_add_u32_e32 v163, v2, v134
	v_add_u32_e32 v162, v4, v134
	v_add_u32_e32 v161, v5, v134
	v_add_u32_e32 v160, v6, v134
	v_add_u32_e32 v17, s1, v156
	v_add_u32_e32 v16, s1, v157
	s_cbranch_scc1 .LBB0_690
	ds_read_b128 v[4:7], v163 offset:4096
	ds_read_b128 v[188:191], v162 offset:4096
	ds_read_b128 v[192:195], v161 offset:4096
	ds_read_b128 v[202:205], v160 offset:4096
	s_and_b32 s0, s10, 0xe0
	v_or_b32_e32 v2, s0, v129
	v_cvt_f32_ubyte0_e32 v2, v2
	v_and_b32_e32 v2, 0x7fff0000, v2
	v_or_b32_sdwa v2, v2, v159 dst_sel:DWORD dst_unused:UNUSED_PAD src0_sel:DWORD src1_sel:WORD_1
	v_cndmask_b32_e64 v210, 0, v2, s[22:23]
	s_or_b32 s0, s9, 63
	s_cmp_lt_u32 s16, s0
	s_waitcnt lgkmcnt(3)
	s_setprio 1
	v_mfma_f32_32x32x16_bf16 v[82:97], v[4:7], v[106:109], 0
	s_cselect_b64 s[0:1], -1, 0
	s_sub_i32 s11, s16, s10
	s_cmp_gt_i32 s11, 0x3fffffe0
	v_add3_u32 v164, v16, v135, s69
	s_cselect_b64 s[12:13], -1, 0
	s_or_b64 s[0:1], s[0:1], s[12:13]
	s_and_b64 vcc, exec, s[0:1]
	s_waitcnt lgkmcnt(2)
	v_mfma_f32_32x32x16_bf16 v[82:97], v[188:191], v[98:101], v[82:97]
	s_waitcnt lgkmcnt(1)
	v_mfma_f32_32x32x16_bf16 v[82:97], v[192:195], v[102:105], v[82:97]
	s_waitcnt lgkmcnt(0)
	v_mfma_f32_32x32x16_bf16 v[82:97], v[202:205], v[110:113], v[82:97]
	v_mfma_f32_32x32x16_bf16 v[82:97], v[210:213], v[114:117], v[82:97]
	s_setprio 0
	v_add3_u32 v2, v17, v135, s69
	ds_read_b64_tr_b16 v[118:119], v2
	ds_read_b64_tr_b16 v[120:121], v2 offset:1024
	ds_read_b64_tr_b16 v[12:13], v164
	ds_read_b64_tr_b16 v[14:15], v164 offset:1024
	ds_read_b64_tr_b16 v[8:9], v2 offset:2048
	ds_read_b64_tr_b16 v[10:11], v2 offset:3072
	ds_read_b64_tr_b16 v[4:5], v164 offset:2048
	ds_read_b64_tr_b16 v[6:7], v164 offset:3072
	s_cbranch_vccnz .LBB0_685
	v_cndmask_b32_e64 v2, 0, 1, s[38:39]
	v_cmp_ne_u32_e32 vcc, 0, v2
	s_cmp_lg_u64 vcc, exec
	s_cselect_b64 s[0:1], -1, 0
	s_cbranch_scc0 .LBB0_687
	v_cndmask_b32_e64 v82, v197, v82, s[38:39]
	v_cndmask_b32_e64 v83, v197, v83, s[38:39]
	v_cndmask_b32_e64 v84, v197, v84, s[38:39]
	v_cndmask_b32_e64 v85, v197, v85, s[38:39]
	v_cndmask_b32_e64 v86, v197, v86, s[38:39]
	v_cndmask_b32_e64 v87, v197, v87, s[38:39]
	v_cndmask_b32_e64 v88, v197, v88, s[38:39]
	v_cndmask_b32_e64 v89, v197, v89, s[38:39]
	v_cndmask_b32_e64 v90, v197, v90, s[38:39]
	v_cndmask_b32_e64 v91, v197, v91, s[38:39]
	v_cndmask_b32_e64 v92, v197, v92, s[38:39]
	v_cndmask_b32_e64 v93, v197, v93, s[38:39]
	v_cndmask_b32_e64 v94, v197, v94, s[38:39]
	v_cndmask_b32_e64 v95, v197, v95, s[38:39]
	v_cndmask_b32_e64 v96, v197, v96, s[38:39]
	v_cndmask_b32_e64 v97, v197, v97, s[38:39]
	s_branch .LBB0_687

.LBB0_689:
	v_mul_f32_e32 v2, 0xbfb8aa3b, v158
	v_fmamk_f32 v82, v82, 0x3fb8aa3b, v2
	v_fmamk_f32 v83, v83, 0x3fb8aa3b, v2
	v_exp_f32_e32 v82, v82
	v_exp_f32_e32 v83, v83
	v_fmamk_f32 v84, v84, 0x3fb8aa3b, v2
	v_fmamk_f32 v85, v85, 0x3fb8aa3b, v2
	v_exp_f32_e32 v84, v84
	v_exp_f32_e32 v85, v85
	v_fmamk_f32 v86, v86, 0x3fb8aa3b, v2
	v_fmamk_f32 v87, v87, 0x3fb8aa3b, v2
	v_fmamk_f32 v88, v88, 0x3fb8aa3b, v2
	v_fmamk_f32 v89, v89, 0x3fb8aa3b, v2
	v_pk_add_f32 v[164:165], v[82:83], 0 op_sel_hi:[1,0]
	v_exp_f32_e32 v86, v86
	v_exp_f32_e32 v87, v87
	v_exp_f32_e32 v88, v88
	v_exp_f32_e32 v89, v89
	v_pk_add_f32 v[164:165], v[84:85], v[164:165]
	v_cvt_pk_bf16_f32 v82, v82, v83
	v_cvt_pk_bf16_f32 v83, v84, v85
	v_cvt_pk_bf16_f32 v84, v86, v87
	v_cvt_pk_bf16_f32 v85, v88, v89
	v_fmamk_f32 v90, v90, 0x3fb8aa3b, v2
	s_waitcnt lgkmcnt(0)
	s_setprio 1
	v_mfma_f32_32x32x16_bf16 v[66:81], v[118:121], v[82:85], v[66:81]
	v_fmamk_f32 v91, v91, 0x3fb8aa3b, v2
	v_exp_f32_e32 v90, v90
	v_exp_f32_e32 v91, v91
	v_fmamk_f32 v92, v92, 0x3fb8aa3b, v2
	v_fmamk_f32 v93, v93, 0x3fb8aa3b, v2
	v_exp_f32_e32 v92, v92
	v_exp_f32_e32 v93, v93
	v_mfma_f32_32x32x16_bf16 v[50:65], v[12:15], v[82:85], v[50:65]
	v_fmamk_f32 v94, v94, 0x3fb8aa3b, v2
	v_fmamk_f32 v95, v95, 0x3fb8aa3b, v2
	v_fmamk_f32 v96, v96, 0x3fb8aa3b, v2
	v_fmac_f32_e32 v2, 0x3fb8aa3b, v97
	v_exp_f32_e32 v94, v94
	v_exp_f32_e32 v95, v95
	v_exp_f32_e32 v96, v96
	v_exp_f32_e32 v97, v2
	v_pk_add_f32 v[164:165], v[86:87], v[164:165]
	v_cvt_pk_bf16_f32 v12, v90, v91
	v_cvt_pk_bf16_f32 v13, v92, v93
	v_cvt_pk_bf16_f32 v14, v94, v95
	v_cvt_pk_bf16_f32 v15, v96, v97
	s_nop 0
	v_mfma_f32_32x32x16_bf16 v[66:81], v[8:11], v[12:15], v[66:81]
	v_add_f32_e64 v164, v88, v164
	v_add_f32_e64 v165, v89, v165
	v_add_f32_e64 v164, v90, v164
	v_add_f32_e64 v165, v91, v165
	v_add_f32_e64 v164, v92, v164
	v_add_f32_e64 v165, v93, v165
	v_pk_add_f32 v[164:165], v[94:95], v[164:165]
	v_mfma_f32_32x32x16_bf16 v[50:65], v[4:7], v[12:15], v[50:65]
	s_setprio 0
	v_add_f32_e64 v164, v96, v164
	v_add_f32_e64 v165, v97, v165
	v_add_f32_e32 v2, v164, v165
	v_add_f32_e32 v144, v144, v2
.LBB0_690:
	s_cmp_gt_i32 s9, s6
	s_cbranch_scc1 .LBB0_669
	ds_read_b128 v[4:7], v163
	ds_read_b128 v[188:191], v162
	ds_read_b128 v[192:195], v161
	ds_read_b128 v[202:205], v160
	s_and_b32 s0, s9, 0xc0
	v_or_b32_e32 v2, s0, v129
	v_cvt_f32_ubyte0_e32 v2, v2
	v_and_b32_e32 v2, 0x7fff0000, v2
	v_or_b32_sdwa v2, v2, v159 dst_sel:DWORD dst_unused:UNUSED_PAD src0_sel:DWORD src1_sel:WORD_1
	v_cndmask_b32_e64 v210, 0, v2, s[22:23]
	s_or_b32 s0, s9, 31
	s_cmp_lt_i32 s16, s0
	s_waitcnt lgkmcnt(3)
	s_setprio 1
	v_mfma_f32_32x32x16_bf16 v[82:97], v[4:7], v[106:109], 0
	s_cselect_b64 s[0:1], -1, 0
	s_sub_i32 s10, s16, s9
	s_cmp_gt_i32 s10, 0x3fffffe0
	v_add3_u32 v16, v16, v135, s67
	s_cselect_b64 s[10:11], -1, 0
	s_or_b64 s[0:1], s[0:1], s[10:11]
	s_and_b64 vcc, exec, s[0:1]
	s_waitcnt lgkmcnt(2)
	v_mfma_f32_32x32x16_bf16 v[82:97], v[188:191], v[98:101], v[82:97]
	s_waitcnt lgkmcnt(1)
	v_mfma_f32_32x32x16_bf16 v[82:97], v[192:195], v[102:105], v[82:97]
	s_waitcnt lgkmcnt(0)
	v_mfma_f32_32x32x16_bf16 v[82:97], v[202:205], v[110:113], v[82:97]
	v_mfma_f32_32x32x16_bf16 v[82:97], v[210:213], v[114:117], v[82:97]
	s_setprio 0
	v_add3_u32 v2, v17, v135, s67
	ds_read_b64_tr_b16 v[118:119], v2
	ds_read_b64_tr_b16 v[120:121], v2 offset:1024
	ds_read_b64_tr_b16 v[12:13], v16
	ds_read_b64_tr_b16 v[14:15], v16 offset:1024
	ds_read_b64_tr_b16 v[8:9], v2 offset:2048
	ds_read_b64_tr_b16 v[10:11], v2 offset:3072
	ds_read_b64_tr_b16 v[4:5], v16 offset:2048
	ds_read_b64_tr_b16 v[6:7], v16 offset:3072
	s_cbranch_vccnz .LBB0_693
	v_cndmask_b32_e64 v2, 0, 1, s[38:39]
	v_cmp_ne_u32_e32 vcc, 0, v2
	s_cmp_lg_u64 vcc, exec
	s_cselect_b64 s[0:1], -1, 0
	s_cbranch_scc0 .LBB0_695
	v_cndmask_b32_e64 v82, v197, v82, s[38:39]
	v_cndmask_b32_e64 v83, v197, v83, s[38:39]
	v_cndmask_b32_e64 v84, v197, v84, s[38:39]
	v_cndmask_b32_e64 v85, v197, v85, s[38:39]
	v_cndmask_b32_e64 v86, v197, v86, s[38:39]
	v_cndmask_b32_e64 v87, v197, v87, s[38:39]
	v_cndmask_b32_e64 v88, v197, v88, s[38:39]
	v_cndmask_b32_e64 v89, v197, v89, s[38:39]
	v_cndmask_b32_e64 v90, v197, v90, s[38:39]
	v_cndmask_b32_e64 v91, v197, v91, s[38:39]
	v_cndmask_b32_e64 v92, v197, v92, s[38:39]
	v_cndmask_b32_e64 v93, v197, v93, s[38:39]
	v_cndmask_b32_e64 v94, v197, v94, s[38:39]
	v_cndmask_b32_e64 v95, v197, v95, s[38:39]
	v_cndmask_b32_e64 v96, v197, v96, s[38:39]
	v_cndmask_b32_e64 v97, v197, v97, s[38:39]
	s_branch .LBB0_695

.LBB0_763:
	s_or_b64 exec, exec, s[0:1]
	v_mov_b32_e32 v4, v0
	s_nop 0
	v_readfirstlane_b32 s15, v4
	s_ashr_i32 s14, s15, 6
	s_cmp_lt_i32 s14, 4
	s_cbranch_scc1 .LBB0_765
	s_nop 0

.LBB0_770:
	v_mul_f32_e32 v2, 0xbfb8aa3b, v113
	v_fmamk_f32 v16, v50, 0x3fb8aa3b, v2
	v_fmamk_f32 v50, v52, 0x3fb8aa3b, v2
	v_exp_f32_e32 v52, v50
	v_fmamk_f32 v50, v53, 0x3fb8aa3b, v2
	v_exp_f32_e32 v53, v50
	v_fmamk_f32 v50, v54, 0x3fb8aa3b, v2
	v_exp_f32_e32 v54, v50
	v_fmamk_f32 v50, v55, 0x3fb8aa3b, v2
	v_exp_f32_e32 v55, v50
	v_fmamk_f32 v50, v56, 0x3fb8aa3b, v2
	v_exp_f32_e32 v56, v50
	v_fmamk_f32 v50, v57, 0x3fb8aa3b, v2
	v_exp_f32_e32 v57, v50
	v_fmamk_f32 v50, v58, 0x3fb8aa3b, v2
	v_exp_f32_e32 v58, v50
	v_fmamk_f32 v50, v59, 0x3fb8aa3b, v2
	v_fmamk_f32 v17, v51, 0x3fb8aa3b, v2
	v_exp_f32_e32 v59, v50
	v_fmamk_f32 v50, v60, 0x3fb8aa3b, v2
	v_exp_f32_e32 v16, v16
	v_exp_f32_e32 v17, v17
	v_exp_f32_e32 v60, v50
	v_fmamk_f32 v50, v61, 0x3fb8aa3b, v2
	v_exp_f32_e32 v61, v50
	v_fmamk_f32 v50, v62, 0x3fb8aa3b, v2
	v_exp_f32_e32 v62, v50
	v_fmamk_f32 v50, v63, 0x3fb8aa3b, v2
	v_exp_f32_e32 v63, v50
	v_fmamk_f32 v50, v64, 0x3fb8aa3b, v2
	v_exp_f32_e32 v64, v50
	v_fmac_f32_e32 v2, 0x3fb8aa3b, v65
	v_pk_add_f32 v[50:51], v[16:17], v[52:53]
	v_exp_f32_e32 v65, v2
	v_pk_add_f32 v[244:245], v[54:55], v[56:57]
	v_pk_add_f32 v[50:51], v[58:59], v[50:51]
	v_pk_add_f32 v[244:245], v[60:61], v[244:245]
	v_pk_add_f32 v[50:51], v[62:63], v[50:51]
	v_pk_add_f32 v[244:245], v[64:65], v[244:245]
	s_nop 0
	v_pk_add_f32 v[50:51], v[50:51], v[244:245]
	s_nop 0
	v_add_f32_e32 v2, v50, v51
	v_cvt_pk_bf16_f32 v50, v16, v17
	v_cvt_pk_bf16_f32 v51, v52, v53
	v_cvt_pk_bf16_f32 v52, v54, v55
	v_cvt_pk_bf16_f32 v53, v56, v57
	v_add_f32_e32 v108, v108, v2
	s_waitcnt lgkmcnt(0)
	s_setprio 1
	v_mfma_f32_32x32x16_bf16 v[34:49], v[86:89], v[50:53], v[34:49]
	v_mfma_f32_32x32x16_bf16 v[18:33], v[12:15], v[50:53], v[18:33]
	v_cvt_pk_bf16_f32 v12, v58, v59
	v_cvt_pk_bf16_f32 v13, v60, v61
	v_cvt_pk_bf16_f32 v14, v62, v63
	v_cvt_pk_bf16_f32 v15, v64, v65
	s_nop 0
	v_mfma_f32_32x32x16_bf16 v[34:49], v[8:11], v[12:15], v[34:49]
	v_mfma_f32_32x32x16_bf16 v[18:33], v[4:7], v[12:15], v[18:33]
	s_setprio 0

.Lw_swa_4_done:
.LBB0_780:
	s_cmp_eq_u32 s32, 0
	s_cselect_b32 s84, 0, 1
	s_sub_u32 s32, s32, s84
	s_add_i32 s0, s25, s17
	s_add_i32 s1, s23, s18
	s_add_i32 s1, s1, -1
	s_and_b32 s27, s26, 0xc000
	s_add_i32 s34, s27, 0
	s_ashr_i32 s1, s1, 2
	s_add_i32 s27, s0, 0x7e0
	s_cmp_gt_i32 s27, s19
	v_cvt_f32_i32_e32 v114, s1
	s_cselect_b64 s[28:29], -1, 0
	s_add_i32 s1, s0, 0x7ff
	s_cmp_lt_i32 s1, s20
	s_cselect_b64 s[30:31], -1, 0
	v_add_u32_e32 v2, s34, v104
	v_add_u32_e32 v4, s34, v105
	v_add_u32_e32 v5, s34, v106
	v_add_u32_e32 v6, s34, v107
	s_or_b64 s[28:29], s[28:29], s[30:31]
	s_and_b64 vcc, exec, s[28:29]
	v_add_u32_e32 v118, v2, v103
	v_add_u32_e32 v117, v4, v103
	v_add_u32_e32 v116, v5, v103
	v_add_u32_e32 v115, v6, v103
	v_add_u32_e32 v16, s34, v109
	v_add_u32_e32 v17, s34, v110
	s_barrier
	s_cbranch_vccnz .LBB0_788
	ds_read_b128 v[4:7], v118 offset:4096
	ds_read_b128 v[188:191], v117 offset:4096
	ds_read_b128 v[192:195], v116 offset:4096
	ds_read_b128 v[202:205], v115 offset:4096
	s_and_b32 s27, s27, 0xe0
	v_or_b32_e32 v2, s27, v102
	v_cvt_f32_ubyte0_e32 v2, v2
	v_and_b32_e32 v2, 0x7fff0000, v2
	v_or_b32_sdwa v2, v2, v114 dst_sel:DWORD dst_unused:UNUSED_PAD src0_sel:DWORD src1_sel:WORD_1
	v_cndmask_b32_e64 v246, 0, v2, s[36:37]
	s_cmp_ge_i32 s16, s1
	s_cselect_b64 s[28:29], -1, 0
	s_waitcnt lgkmcnt(3)
	s_setprio 1
	v_mfma_f32_32x32x16_bf16 v[50:65], v[4:7], v[66:69], 0
	s_sub_i32 s1, s15, 32
	s_cmpk_lt_i32 s1, 0x61
	v_add3_u32 v119, v17, v96, s69
	s_cselect_b64 s[30:31], -1, 0
	s_and_b64 s[28:29], s[28:29], s[30:31]
	s_and_b64 vcc, exec, s[28:29]
	s_waitcnt lgkmcnt(2)
	v_mfma_f32_32x32x16_bf16 v[50:65], v[188:191], v[70:73], v[50:65]
	s_waitcnt lgkmcnt(1)
	v_mfma_f32_32x32x16_bf16 v[50:65], v[192:195], v[74:77], v[50:65]
	s_waitcnt lgkmcnt(0)
	v_mfma_f32_32x32x16_bf16 v[50:65], v[202:205], v[78:81], v[50:65]
	v_mfma_f32_32x32x16_bf16 v[50:65], v[246:249], v[82:85], v[50:65]
	s_setprio 0
	v_add3_u32 v2, v16, v96, s69
	ds_read_b64_tr_b16 v[86:87], v2
	ds_read_b64_tr_b16 v[88:89], v2 offset:1024
	ds_read_b64_tr_b16 v[12:13], v119
	ds_read_b64_tr_b16 v[14:15], v119 offset:1024
	ds_read_b64_tr_b16 v[8:9], v2 offset:2048
	ds_read_b64_tr_b16 v[10:11], v2 offset:3072
	ds_read_b64_tr_b16 v[4:5], v119 offset:2048
	ds_read_b64_tr_b16 v[6:7], v119 offset:3072
	s_cbranch_vccnz .LBB0_785
	v_add_u32_e32 v2, s15, v111
	v_subrev_u32_e32 v119, 32, v2
	v_cmp_gt_u32_e32 vcc, s71, v119
	v_add3_u32 v119, v112, s17, 32
	s_nop 5
	v_cndmask_b32_e32 v50, v197, v50, vcc
	v_cmp_lt_u32_e32 vcc, s47, v119
	v_subrev_u32_e32 v119, 34, v2
	s_nop 0
	v_cndmask_b32_e32 v51, v197, v51, vcc
	v_cmp_gt_u32_e32 vcc, s71, v119
	v_subrev_u32_e32 v119, 35, v2
	s_nop 0
	v_cndmask_b32_e32 v52, v197, v52, vcc
	v_cmp_gt_u32_e32 vcc, s71, v119
	v_subrev_u32_e32 v119, 40, v2
	s_nop 0
	v_cndmask_b32_e32 v53, v197, v53, vcc
	v_cmp_gt_u32_e32 vcc, s71, v119
	v_subrev_u32_e32 v119, 41, v2
	s_nop 0
	v_cndmask_b32_e32 v54, v197, v54, vcc
	v_cmp_gt_u32_e32 vcc, s71, v119
	v_subrev_u32_e32 v119, 42, v2
	s_nop 0
	v_cndmask_b32_e32 v55, v197, v55, vcc
	v_cmp_gt_u32_e32 vcc, s71, v119
	v_subrev_u32_e32 v119, 43, v2
	s_nop 0
	v_cndmask_b32_e32 v56, v197, v56, vcc
	v_cmp_gt_u32_e32 vcc, s71, v119
	v_subrev_u32_e32 v119, 48, v2
	s_nop 0
	v_cndmask_b32_e32 v57, v197, v57, vcc
	v_cmp_gt_u32_e32 vcc, s71, v119
	v_subrev_u32_e32 v119, 49, v2
	s_nop 0
	v_cndmask_b32_e32 v58, v197, v58, vcc
	v_cmp_gt_u32_e32 vcc, s71, v119
	v_subrev_u32_e32 v119, 50, v2
	s_nop 0
	v_cndmask_b32_e32 v59, v197, v59, vcc
	v_cmp_gt_u32_e32 vcc, s71, v119
	v_subrev_u32_e32 v119, 51, v2
	s_nop 0
	v_cndmask_b32_e32 v60, v197, v60, vcc
	v_cmp_gt_u32_e32 vcc, s71, v119
	v_subrev_u32_e32 v119, 56, v2
	s_nop 0
	v_cndmask_b32_e32 v61, v197, v61, vcc
	v_cmp_gt_u32_e32 vcc, s71, v119
	v_subrev_u32_e32 v119, 57, v2
	s_nop 0
	v_cndmask_b32_e32 v62, v197, v62, vcc
	v_cmp_gt_u32_e32 vcc, s71, v119
	v_subrev_u32_e32 v119, 58, v2
	v_subrev_u32_e32 v2, 59, v2
	v_cndmask_b32_e32 v63, v197, v63, vcc
	v_cmp_gt_u32_e32 vcc, s71, v119
	s_nop 1
	v_cndmask_b32_e32 v64, v197, v64, vcc
	v_cmp_gt_u32_e32 vcc, s71, v2
	s_nop 1
	v_cndmask_b32_e32 v65, v197, v65, vcc

.LBB0_787:
	v_mul_f32_e32 v2, 0xbfb8aa3b, v113
	v_fmamk_f32 v50, v50, 0x3fb8aa3b, v2
	v_fmamk_f32 v51, v51, 0x3fb8aa3b, v2
	v_exp_f32_e32 v50, v50
	v_exp_f32_e32 v51, v51
	v_fmamk_f32 v52, v52, 0x3fb8aa3b, v2
	v_fmamk_f32 v53, v53, 0x3fb8aa3b, v2
	v_exp_f32_e32 v52, v52
	v_exp_f32_e32 v53, v53
	v_fmamk_f32 v54, v54, 0x3fb8aa3b, v2
	v_fmamk_f32 v55, v55, 0x3fb8aa3b, v2
	v_fmamk_f32 v56, v56, 0x3fb8aa3b, v2
	v_fmamk_f32 v57, v57, 0x3fb8aa3b, v2
	v_pk_add_f32 v[120:121], v[50:51], 0 op_sel_hi:[1,0]
	v_exp_f32_e32 v54, v54
	v_exp_f32_e32 v55, v55
	v_exp_f32_e32 v56, v56
	v_exp_f32_e32 v57, v57
	v_pk_add_f32 v[120:121], v[52:53], v[120:121]
	v_cvt_pk_bf16_f32 v50, v50, v51
	v_cvt_pk_bf16_f32 v51, v52, v53
	v_cvt_pk_bf16_f32 v52, v54, v55
	v_cvt_pk_bf16_f32 v53, v56, v57
	v_fmamk_f32 v58, v58, 0x3fb8aa3b, v2
	s_waitcnt lgkmcnt(0)
	s_setprio 1
	v_mfma_f32_32x32x16_bf16 v[34:49], v[86:89], v[50:53], v[34:49]
	v_fmamk_f32 v59, v59, 0x3fb8aa3b, v2
	v_exp_f32_e32 v58, v58
	v_exp_f32_e32 v59, v59
	v_fmamk_f32 v60, v60, 0x3fb8aa3b, v2
	v_fmamk_f32 v61, v61, 0x3fb8aa3b, v2
	v_exp_f32_e32 v60, v60
	v_exp_f32_e32 v61, v61
	v_mfma_f32_32x32x16_bf16 v[18:33], v[12:15], v[50:53], v[18:33]
	v_fmamk_f32 v62, v62, 0x3fb8aa3b, v2
	v_fmamk_f32 v63, v63, 0x3fb8aa3b, v2
	v_fmamk_f32 v64, v64, 0x3fb8aa3b, v2
	v_fmac_f32_e32 v2, 0x3fb8aa3b, v65
	v_exp_f32_e32 v62, v62
	v_exp_f32_e32 v63, v63
	v_exp_f32_e32 v64, v64
	v_exp_f32_e32 v65, v2
	v_pk_add_f32 v[120:121], v[54:55], v[120:121]
	v_cvt_pk_bf16_f32 v12, v58, v59
	v_cvt_pk_bf16_f32 v13, v60, v61
	v_cvt_pk_bf16_f32 v14, v62, v63
	v_cvt_pk_bf16_f32 v15, v64, v65
	s_nop 0
	v_mfma_f32_32x32x16_bf16 v[34:49], v[8:11], v[12:15], v[34:49]
	v_add_f32_e64 v120, v56, v120
	v_add_f32_e64 v121, v57, v121
	v_add_f32_e64 v120, v58, v120
	v_add_f32_e64 v121, v59, v121
	v_add_f32_e64 v120, v60, v120
	v_add_f32_e64 v121, v61, v121
	v_pk_add_f32 v[120:121], v[62:63], v[120:121]
	v_mfma_f32_32x32x16_bf16 v[18:33], v[4:7], v[12:15], v[18:33]
	s_setprio 0
	v_add_f32_e64 v120, v64, v120
	v_add_f32_e64 v121, v65, v121
	v_add_f32_e32 v2, v120, v121
	v_add_f32_e32 v108, v108, v2

.Lring_issue_skip_1:
	s_add_i32 s1, s0, 0x7c0
	s_cmp_gt_i32 s1, s19
	s_cselect_b64 s[28:29], -1, 0
	s_addk_i32 s0, 0x7df
	s_cmp_lt_i32 s0, s20
	s_cselect_b64 s[30:31], -1, 0
	s_or_b64 s[28:29], s[28:29], s[30:31]
	s_and_b64 vcc, exec, s[28:29]
	s_cbranch_vccnz .LBB0_771
	ds_read_b128 v[4:7], v118
	ds_read_b128 v[188:191], v117
	ds_read_b128 v[192:195], v116
	ds_read_b128 v[202:205], v115
	s_and_b32 s1, s1, 0xc0
	v_or_b32_e32 v2, s1, v102
	v_cvt_f32_ubyte0_e32 v2, v2
	v_and_b32_e32 v2, 0x7fff0000, v2
	v_or_b32_sdwa v2, v2, v114 dst_sel:DWORD dst_unused:UNUSED_PAD src0_sel:DWORD src1_sel:WORD_1
	v_cndmask_b32_e64 v246, 0, v2, s[36:37]
	s_cmp_ge_i32 s16, s0
	s_cselect_b64 s[0:1], -1, 0
	s_waitcnt lgkmcnt(3)
	s_setprio 1
	v_mfma_f32_32x32x16_bf16 v[50:65], v[4:7], v[66:69], 0
	s_cmpk_lt_i32 s15, 0x61
	s_cselect_b64 s[28:29], -1, 0
	s_and_b64 s[0:1], s[0:1], s[28:29]
	s_and_b64 vcc, exec, s[0:1]
	s_waitcnt lgkmcnt(2)
	v_mfma_f32_32x32x16_bf16 v[50:65], v[188:191], v[70:73], v[50:65]
	s_waitcnt lgkmcnt(1)
	v_mfma_f32_32x32x16_bf16 v[50:65], v[192:195], v[74:77], v[50:65]
	s_waitcnt lgkmcnt(0)
	v_mfma_f32_32x32x16_bf16 v[50:65], v[202:205], v[78:81], v[50:65]
	v_mfma_f32_32x32x16_bf16 v[50:65], v[246:249], v[82:85], v[50:65]
	s_setprio 0
	v_add3_u32 v2, v16, v96, s67
	v_add3_u32 v16, v17, v96, s67
	ds_read_b64_tr_b16 v[86:87], v2
	ds_read_b64_tr_b16 v[88:89], v2 offset:1024
	ds_read_b64_tr_b16 v[12:13], v16
	ds_read_b64_tr_b16 v[14:15], v16 offset:1024
	ds_read_b64_tr_b16 v[8:9], v2 offset:2048
	ds_read_b64_tr_b16 v[10:11], v2 offset:3072
	ds_read_b64_tr_b16 v[4:5], v16 offset:2048
	ds_read_b64_tr_b16 v[6:7], v16 offset:3072
	s_cbranch_vccnz .LBB0_791
	v_add_u32_e32 v2, s15, v111
	v_cmp_gt_u32_e32 vcc, s71, v2
	v_add_u32_e32 v16, s17, v112
	s_nop 5
	v_cndmask_b32_e32 v50, v197, v50, vcc
	v_cmp_lt_u32_e32 vcc, s47, v16
	v_add_u32_e32 v16, -2, v2
	s_nop 0
	v_cndmask_b32_e32 v51, v197, v51, vcc
	v_cmp_gt_u32_e32 vcc, s71, v16
	v_add_u32_e32 v16, -3, v2
	s_nop 0
	v_cndmask_b32_e32 v52, v197, v52, vcc
	v_cmp_gt_u32_e32 vcc, s71, v16
	v_add_u32_e32 v16, -8, v2
	s_nop 0
	v_cndmask_b32_e32 v53, v197, v53, vcc
	v_cmp_gt_u32_e32 vcc, s71, v16
	v_add_u32_e32 v16, -9, v2
	s_nop 0
	v_cndmask_b32_e32 v54, v197, v54, vcc
	v_cmp_gt_u32_e32 vcc, s71, v16
	v_add_u32_e32 v16, -10, v2
	s_nop 0
	v_cndmask_b32_e32 v55, v197, v55, vcc
	v_cmp_gt_u32_e32 vcc, s71, v16
	v_add_u32_e32 v16, -11, v2
	s_nop 0
	v_cndmask_b32_e32 v56, v197, v56, vcc
	v_cmp_gt_u32_e32 vcc, s71, v16
	v_add_u32_e32 v16, -16, v2
	s_nop 0
	v_cndmask_b32_e32 v57, v197, v57, vcc
	v_cmp_gt_u32_e32 vcc, s71, v16
	v_subrev_u32_e32 v16, 17, v2
	s_nop 0
	v_cndmask_b32_e32 v58, v197, v58, vcc
	v_cmp_gt_u32_e32 vcc, s71, v16
	v_subrev_u32_e32 v16, 18, v2
	s_nop 0
	v_cndmask_b32_e32 v59, v197, v59, vcc
	v_cmp_gt_u32_e32 vcc, s71, v16
	v_subrev_u32_e32 v16, 19, v2
	s_nop 0
	v_cndmask_b32_e32 v60, v197, v60, vcc
	v_cmp_gt_u32_e32 vcc, s71, v16
	v_subrev_u32_e32 v16, 24, v2
	s_nop 0
	v_cndmask_b32_e32 v61, v197, v61, vcc
	v_cmp_gt_u32_e32 vcc, s71, v16
	v_subrev_u32_e32 v16, 25, v2
	s_nop 0
	v_cndmask_b32_e32 v62, v197, v62, vcc
	v_cmp_gt_u32_e32 vcc, s71, v16
	v_subrev_u32_e32 v16, 26, v2
	v_subrev_u32_e32 v2, 27, v2
	v_cndmask_b32_e32 v63, v197, v63, vcc
	v_cmp_gt_u32_e32 vcc, s71, v16
	s_nop 1
	v_cndmask_b32_e32 v64, v197, v64, vcc
	v_cmp_gt_u32_e32 vcc, s71, v2
	s_nop 1
	v_cndmask_b32_e32 v65, v197, v65, vcc
